# speedup vs baseline: 1.0086x; 1.0086x over previous
_Z6k_prepPKfS0_P6__halfS2_Pi:
	s_mov_b32 s12, 0
	s_mov_b64 s[14:15], s[0:1]
	s_mov_b32 s13, s2
	v_mov_b32_e32 v6, v0
.Lx_prep_top:
	s_cmpk_gt_i32 s2, 0x43
	s_mov_b64 s[4:5], -1
	s_cbranch_scc0 .LBB0_12
	s_lshl_b32 s3, s2, 8
	s_cmpk_gt_u32 s2, 0x54
	s_cbranch_scc0 .LBB0_5
	v_add_u32_e32 v1, s3, v0
	v_add_u32_e32 v2, 0xffffab00, v1
	s_movk_i32 s4, 0x3100
	v_cmp_gt_i32_e32 vcc, s4, v2
	s_and_saveexec_b64 s[4:5], vcc
	s_cbranch_execz .LBB0_4
	s_load_dwordx2 s[6:7], s[0:1], 0x20
	v_mov_b32_e32 v3, 0
	s_waitcnt lgkmcnt(0)
	v_lshl_add_u64 v[4:5], v[2:3], 2, s[6:7]
	global_store_dword v[4:5], v3, off

.LBB0_17:
	s_mov_b64 exec, -1
	s_cmp_lg_u32 s12, 0
	s_cbranch_scc1 .Lx_prep_done
	s_mov_b32 s12, 1
	s_mov_b64 s[0:1], s[14:15]
	s_mov_b32 s2, s13
	v_mov_b32_e32 v0, v6
	s_waitcnt vmcnt(0) lgkmcnt(0)
	s_branch .Lx_prep_top

	.amdhsa_kernel _Z6k_prepPKfS0_P6__halfS2_Pi
		.amdhsa_group_segment_fixed_size 0
		.amdhsa_private_segment_fixed_size 0
		.amdhsa_kernarg_size 40
		.amdhsa_user_sgpr_count 2
		.amdhsa_user_sgpr_dispatch_ptr 0
		.amdhsa_user_sgpr_queue_ptr 0
		.amdhsa_user_sgpr_kernarg_segment_ptr 1
		.amdhsa_user_sgpr_dispatch_id 0
		.amdhsa_user_sgpr_kernarg_preload_length 0
		.amdhsa_user_sgpr_kernarg_preload_offset 0
		.amdhsa_user_sgpr_private_segment_size 0
		.amdhsa_uses_dynamic_stack 0
		.amdhsa_enable_private_segment 0
		.amdhsa_system_sgpr_workgroup_id_x 1
		.amdhsa_system_sgpr_workgroup_id_y 0
		.amdhsa_system_sgpr_workgroup_id_z 0
		.amdhsa_system_sgpr_workgroup_info 0
		.amdhsa_system_vgpr_workitem_id 0
		.amdhsa_next_free_vgpr 7
		.amdhsa_next_free_sgpr 16
		.amdhsa_accum_offset 8
		.amdhsa_reserve_vcc 1
		.amdhsa_float_round_mode_32 0
		.amdhsa_float_round_mode_16_64 0
		.amdhsa_float_denorm_mode_32 3
		.amdhsa_float_denorm_mode_16_64 3
		.amdhsa_dx10_clamp 1
		.amdhsa_ieee_mode 1
		.amdhsa_fp16_overflow 0
		.amdhsa_tg_split 0
		.amdhsa_exception_fp_ieee_invalid_op 0
		.amdhsa_exception_fp_denorm_src 0
		.amdhsa_exception_fp_ieee_div_zero 0
		.amdhsa_exception_fp_ieee_overflow 0
		.amdhsa_exception_fp_ieee_underflow 0
		.amdhsa_exception_fp_ieee_inexact 0
		.amdhsa_exception_int_div_zero 0
	.end_amdhsa_kernel

amdhsa.kernels:
  - .agpr_count:     0
    .args:
      - .actual_access:  read_only
        .address_space:  global
        .offset:         0
        .size:           8
        .value_kind:     global_buffer
      - .actual_access:  read_only
        .address_space:  global
        .offset:         8
        .size:           8
        .value_kind:     global_buffer
      - .actual_access:  write_only
        .address_space:  global
        .offset:         16
        .size:           8
        .value_kind:     global_buffer
      - .actual_access:  write_only
        .address_space:  global
        .offset:         24
        .size:           8
        .value_kind:     global_buffer
      - .actual_access:  write_only
        .address_space:  global
        .offset:         32
        .size:           8
        .value_kind:     global_buffer
    .group_segment_fixed_size: 0
    .kernarg_segment_align: 8
    .kernarg_segment_size: 40
    .language:       OpenCL C
    .language_version:
      - 2
      - 0
    .max_flat_workgroup_size: 256
    .name:           _Z6k_prepPKfS0_P6__halfS2_Pi
    .private_segment_fixed_size: 0
    .sgpr_count:     22
    .sgpr_spill_count: 0
    .symbol:         _Z6k_prepPKfS0_P6__halfS2_Pi.kd
    .uniform_work_group_size: 1
    .uses_dynamic_stack: false
    .vgpr_count:     7
    .vgpr_spill_count: 0
    .wavefront_size: 64
  - .agpr_count:     0
    .args:
      - .actual_access:  read_only
        .address_space:  global
        .offset:         0
        .size:           8
        .value_kind:     global_buffer
      - .actual_access:  read_only
        .address_space:  global
        .offset:         8
        .size:           8
        .value_kind:     global_buffer
      - .address_space:  global
        .offset:         16
        .size:           8
        .value_kind:     global_buffer
      - .actual_access:  write_only
        .address_space:  global
        .offset:         24
        .size:           8
        .value_kind:     global_buffer
      - .actual_access:  write_only
        .address_space:  global
        .offset:         32
        .size:           8
        .value_kind:     global_buffer
      - .actual_access:  read_only
        .address_space:  global
        .offset:         40
        .size:           8
        .value_kind:     global_buffer
      - .actual_access:  read_only
        .address_space:  global
        .offset:         48
        .size:           8
        .value_kind:     global_buffer
      - .actual_access:  read_only
        .address_space:  global
        .offset:         56
        .size:           8
        .value_kind:     global_buffer
      - .actual_access:  read_only
        .address_space:  global
        .offset:         64
        .size:           8
        .value_kind:     global_buffer
      - .actual_access:  write_only
        .address_space:  global
        .offset:         72
        .size:           8
        .value_kind:     global_buffer
      - .actual_access:  read_only
        .address_space:  global
        .offset:         80
        .size:           8
        .value_kind:     global_buffer
      - .actual_access:  write_only
        .address_space:  global
        .offset:         88
        .size:           8
        .value_kind:     global_buffer
    .group_segment_fixed_size: 53248
    .kernarg_segment_align: 8
    .kernarg_segment_size: 96
    .language:       OpenCL C
    .language_version:
      - 2
      - 0
    .max_flat_workgroup_size: 256
    .name:           _Z15k_scatter_gemm1PKiS0_PiPjPyPKfPK6__halfS5_S5_PS6_PfSA_
    .private_segment_fixed_size: 0
    .sgpr_count:     32
    .sgpr_spill_count: 0
    .symbol:         _Z15k_scatter_gemm1PKiS0_PiPjPyPKfPK6__halfS5_S5_PS6_PfSA_.kd
    .uniform_work_group_size: 1
    .uses_dynamic_stack: false
    .vgpr_count:     146
    .vgpr_spill_count: 0
    .wavefront_size: 64
  - .agpr_count:     0
    .args:
      - .actual_access:  read_only
        .address_space:  global
        .offset:         0
        .size:           8
        .value_kind:     global_buffer
      - .actual_access:  read_only
        .address_space:  global
        .offset:         8
        .size:           8
        .value_kind:     global_buffer
      - .actual_access:  read_only
        .address_space:  global
        .offset:         16
        .size:           8
        .value_kind:     global_buffer
      - .actual_access:  write_only
        .address_space:  global
        .offset:         24
        .size:           8
        .value_kind:     global_buffer
      - .actual_access:  write_only
        .address_space:  global
        .offset:         32
        .size:           8
        .value_kind:     global_buffer
      - .actual_access:  write_only
        .address_space:  global
        .offset:         40
        .size:           8
        .value_kind:     global_buffer
      - .actual_access:  write_only
        .address_space:  global
        .offset:         48
        .size:           8
        .value_kind:     global_buffer
      - .actual_access:  read_only
        .address_space:  global
        .offset:         56
        .size:           8
        .value_kind:     global_buffer
      - .actual_access:  read_only
        .address_space:  global
        .offset:         64
        .size:           8
        .value_kind:     global_buffer
      - .actual_access:  read_only
        .address_space:  global
        .offset:         72
        .size:           8
        .value_kind:     global_buffer
      - .actual_access:  read_only
        .address_space:  global
        .offset:         80
        .size:           8
        .value_kind:     global_buffer
      - .actual_access:  write_only
        .address_space:  global
        .offset:         88
        .size:           8
        .value_kind:     global_buffer
      - .actual_access:  read_only
        .address_space:  global
        .offset:         96
        .size:           8
        .value_kind:     global_buffer
      - .actual_access:  write_only
        .address_space:  global
        .offset:         104
        .size:           8
        .value_kind:     global_buffer
    .group_segment_fixed_size: 53248
    .kernarg_segment_align: 8
    .kernarg_segment_size: 112
    .language:       OpenCL C
    .language_version:
      - 2
      - 0
    .max_flat_workgroup_size: 256
    .name:           _Z12k_fine_gemm1PKjPKyPKiPiS5_S5_S5_PKfPK6__halfS7_S7_PS8_PfSC_
    .private_segment_fixed_size: 0
    .sgpr_count:     102
    .sgpr_spill_count: 0
    .symbol:         _Z12k_fine_gemm1PKjPKyPKiPiS5_S5_S5_PKfPK6__halfS7_S7_PS8_PfSC_.kd
    .uniform_work_group_size: 1
    .uses_dynamic_stack: false
    .vgpr_count:     144
    .vgpr_spill_count: 0
    .wavefront_size: 64
  - .agpr_count:     0
    .args:
      - .actual_access:  read_only
        .address_space:  global
        .offset:         0
        .size:           8
        .value_kind:     global_buffer
      - .actual_access:  read_only
        .address_space:  global
        .offset:         8
        .size:           8
        .value_kind:     global_buffer
      - .actual_access:  read_only
        .address_space:  global
        .offset:         16
        .size:           8
        .value_kind:     global_buffer
      - .actual_access:  read_only
        .address_space:  global
        .offset:         24
        .size:           8
        .value_kind:     global_buffer
      - .actual_access:  read_only
        .address_space:  global
        .offset:         32
        .size:           8
        .value_kind:     global_buffer
      - .actual_access:  read_only
        .address_space:  global
        .offset:         40
        .size:           8
        .value_kind:     global_buffer
      - .actual_access:  read_only
        .address_space:  global
        .offset:         48
        .size:           8
        .value_kind:     global_buffer
      - .actual_access:  read_only
        .address_space:  global
        .offset:         56
        .size:           8
        .value_kind:     global_buffer
      - .actual_access:  read_only
        .address_space:  global
        .offset:         64
        .size:           8
        .value_kind:     global_buffer
      - .actual_access:  write_only
        .address_space:  global
        .offset:         72
        .size:           8
        .value_kind:     global_buffer
      - .actual_access:  read_only
        .address_space:  global
        .offset:         80
        .size:           8
        .value_kind:     global_buffer
      - .actual_access:  write_only
        .address_space:  global
        .offset:         88
        .size:           8
        .value_kind:     global_buffer
      - .actual_access:  read_only
        .address_space:  global
        .offset:         96
        .size:           8
        .value_kind:     global_buffer
      - .actual_access:  read_only
        .address_space:  global
        .offset:         104
        .size:           8
        .value_kind:     global_buffer
      - .actual_access:  read_only
        .address_space:  global
        .offset:         112
        .size:           8
        .value_kind:     global_buffer
    .group_segment_fixed_size: 5376
    .kernarg_segment_align: 8
    .kernarg_segment_size: 120
    .language:       OpenCL C
    .language_version:
      - 2
      - 0
    .max_flat_workgroup_size: 256
    .name:           _Z6k_agg1PKiS0_PK6__halfPKfS5_S5_S3_S5_S5_PS1_PfS7_S5_S0_S0_
    .private_segment_fixed_size: 0
    .sgpr_count:     43
    .sgpr_spill_count: 0
    .symbol:         _Z6k_agg1PKiS0_PK6__halfPKfS5_S5_S3_S5_S5_PS1_PfS7_S5_S0_S0_.kd
    .uniform_work_group_size: 1
    .uses_dynamic_stack: false
    .vgpr_count:     77
    .vgpr_spill_count: 0
    .wavefront_size: 64
  - .agpr_count:     0
    .args:
      - .actual_access:  read_only
        .address_space:  global
        .offset:         0
        .size:           8
        .value_kind:     global_buffer
      - .actual_access:  read_only
        .address_space:  global
        .offset:         8
        .size:           8
        .value_kind:     global_buffer
      - .actual_access:  read_only
        .address_space:  global
        .offset:         16
        .size:           8
        .value_kind:     global_buffer
      - .actual_access:  read_only
        .address_space:  global
        .offset:         24
        .size:           8
        .value_kind:     global_buffer
      - .actual_access:  read_only
        .address_space:  global
        .offset:         32
        .size:           8
        .value_kind:     global_buffer
      - .actual_access:  read_only
        .address_space:  global
        .offset:         40
        .size:           8
        .value_kind:     global_buffer
      - .actual_access:  write_only
        .address_space:  global
        .offset:         48
        .size:           8
        .value_kind:     global_buffer
      - .actual_access:  read_only
        .address_space:  global
        .offset:         56
        .size:           8
        .value_kind:     global_buffer
      - .actual_access:  read_only
        .address_space:  global
        .offset:         64
        .size:           8
        .value_kind:     global_buffer
      - .actual_access:  read_only
        .address_space:  global
        .offset:         72
        .size:           8
        .value_kind:     global_buffer
    .group_segment_fixed_size: 1024
    .kernarg_segment_align: 8
    .kernarg_segment_size: 80
    .language:       OpenCL C
    .language_version:
      - 2
      - 0
    .max_flat_workgroup_size: 256
    .name:           _Z6k_agg2PKiS0_PK6__halfPKfS5_S5_PfS5_S0_S0_
    .private_segment_fixed_size: 0
    .sgpr_count:     28
    .sgpr_spill_count: 0
    .symbol:         _Z6k_agg2PKiS0_PK6__halfPKfS5_S5_PfS5_S0_S0_.kd
    .uniform_work_group_size: 1
    .uses_dynamic_stack: false
    .vgpr_count:     60
    .vgpr_spill_count: 0
    .wavefront_size: 64
